# grid-barrier spin loops: poll back-off s_sleep 4 instead of 1 (fewer polls beside the stragglers)
# baseline (speedup 1.0000x reference)
.LBB0_42:
	global_load_dword v16, v17, s[76:77] offset:1024 sc1
	s_waitcnt lgkmcnt(0)
	global_load_dword v1, v17, s[76:77] offset:1280 sc1
	global_load_dword v2, v17, s[76:77] offset:1536 sc1
	global_load_dword v3, v17, s[76:77] offset:1792 sc1
	global_load_dword v4, v17, s[76:77] offset:2048 sc1
	global_load_dword v5, v17, s[76:77] offset:2304 sc1
	global_load_dword v6, v17, s[76:77] offset:2560 sc1
	global_load_dword v7, v17, s[76:77] offset:2816 sc1
	global_load_dword v8, v17, s[76:77] offset:3072 sc1
	global_load_dword v9, v17, s[76:77] offset:3328 sc1
	global_load_dword v10, v17, s[76:77] offset:3584 sc1
	global_load_dword v11, v17, s[76:77] offset:3840 sc1
	global_load_dword v12, v17, s[6:7] sc1
	global_load_dword v13, v17, s[8:9] sc1
	global_load_dword v14, v17, s[10:11] sc1
	global_load_dword v15, v17, s[12:13] sc1
	s_mov_b64 s[14:15], -1
	s_mov_b64 s[16:17], -1
	s_waitcnt vmcnt(14)
	v_add_u32_e32 v18, v1, v16
	s_waitcnt vmcnt(13)
	v_add_u32_e32 v18, v18, v2
	s_waitcnt vmcnt(12)
	v_add_u32_e32 v18, v18, v3
	s_waitcnt vmcnt(11)
	v_add_u32_e32 v18, v18, v4
	s_waitcnt vmcnt(10)
	v_add_u32_e32 v18, v18, v5
	s_waitcnt vmcnt(9)
	v_add_u32_e32 v18, v18, v6
	s_waitcnt vmcnt(8)
	v_add_u32_e32 v18, v18, v7
	s_waitcnt vmcnt(7)
	v_add_u32_e32 v18, v18, v8
	s_waitcnt vmcnt(6)
	v_add_u32_e32 v18, v18, v9
	s_waitcnt vmcnt(5)
	v_add_u32_e32 v18, v18, v10
	s_waitcnt vmcnt(4)
	v_add_u32_e32 v18, v18, v11
	s_waitcnt vmcnt(3)
	v_add_u32_e32 v18, v18, v12
	s_waitcnt vmcnt(2)
	v_add_u32_e32 v18, v18, v13
	s_waitcnt vmcnt(1)
	v_add_u32_e32 v18, v18, v14
	s_waitcnt vmcnt(0)
	v_add_u32_e32 v18, v18, v15
	v_cmp_eq_u32_e32 vcc, s33, v18
	s_cbranch_vccnz .LBB0_41
	s_and_b32 s14, s20, 0xff
	s_cmp_eq_u32 s14, 0
	s_mov_b64 s[14:15], -1
	s_mov_b64 s[18:19], -1
	s_sleep 4
	s_cbranch_scc0 .LBB0_46
	global_load_dword v18, v17, s[76:77] offset:512 sc1
	s_waitcnt vmcnt(0)
	v_cmp_eq_u32_e32 vcc, 0, v18
	s_cbranch_vccnz .LBB0_48
	s_mov_b64 s[18:19], 0

.LBB0_60:
	s_and_b32 s20, s25, 0xff
	s_mov_b64 s[18:19], -1
	s_cmp_lg_u32 s20, 0
	s_mov_b64 s[22:23], -1
	s_sleep 4
	s_cbranch_scc1 .LBB0_63
	global_load_dword v3, v1, s[76:77] offset:512 sc1
	s_waitcnt vmcnt(0)
	v_cmp_eq_u32_e32 vcc, 0, v3
	s_cbranch_vccnz .LBB0_65
	s_mov_b64 s[22:23], 0
	s_mov_b64 s[20:21], -1

.LBB0_77:
	s_and_b32 s20, s25, 0xff
	s_cmp_lg_u32 s20, 0
	s_mov_b64 s[22:23], -1
	s_sleep 4
	s_cbranch_scc1 .LBB0_80
	global_load_dword v2, v1, s[12:13] sc1
	s_waitcnt vmcnt(0)
	v_cmp_eq_u32_e32 vcc, 0, v2
	s_cbranch_vccnz .LBB0_82
	s_mov_b64 s[22:23], 0
	s_mov_b64 s[20:21], -1

.LBB0_294:
	global_load_dword v16, v17, s[28:29] offset:1024 sc1
	s_waitcnt lgkmcnt(0)
	global_load_dword v1, v17, s[28:29] offset:1280 sc1
	global_load_dword v2, v17, s[28:29] offset:1536 sc1
	global_load_dword v3, v17, s[28:29] offset:1792 sc1
	global_load_dword v4, v17, s[28:29] offset:2048 sc1
	global_load_dword v5, v17, s[28:29] offset:2304 sc1
	global_load_dword v6, v17, s[28:29] offset:2560 sc1
	global_load_dword v7, v17, s[28:29] offset:2816 sc1
	global_load_dword v8, v17, s[28:29] offset:3072 sc1
	global_load_dword v9, v17, s[28:29] offset:3328 sc1
	global_load_dword v10, v17, s[28:29] offset:3584 sc1
	global_load_dword v11, v17, s[28:29] offset:3840 sc1
	global_load_dword v12, v17, s[4:5] sc1
	global_load_dword v13, v17, s[6:7] sc1
	global_load_dword v14, v17, s[8:9] sc1
	global_load_dword v15, v17, s[10:11] sc1
	s_mov_b64 s[12:13], -1
	s_mov_b64 s[14:15], -1
	s_waitcnt vmcnt(14)
	v_add_u32_e32 v18, v1, v16
	s_waitcnt vmcnt(13)
	v_add_u32_e32 v18, v18, v2
	s_waitcnt vmcnt(12)
	v_add_u32_e32 v18, v18, v3
	s_waitcnt vmcnt(11)
	v_add_u32_e32 v18, v18, v4
	s_waitcnt vmcnt(10)
	v_add_u32_e32 v18, v18, v5
	s_waitcnt vmcnt(9)
	v_add_u32_e32 v18, v18, v6
	s_waitcnt vmcnt(8)
	v_add_u32_e32 v18, v18, v7
	s_waitcnt vmcnt(7)
	v_add_u32_e32 v18, v18, v8
	s_waitcnt vmcnt(6)
	v_add_u32_e32 v18, v18, v9
	s_waitcnt vmcnt(5)
	v_add_u32_e32 v18, v18, v10
	s_waitcnt vmcnt(4)
	v_add_u32_e32 v18, v18, v11
	s_waitcnt vmcnt(3)
	v_add_u32_e32 v18, v18, v12
	s_waitcnt vmcnt(2)
	v_add_u32_e32 v18, v18, v13
	s_waitcnt vmcnt(1)
	v_add_u32_e32 v18, v18, v14
	s_waitcnt vmcnt(0)
	v_add_u32_e32 v18, v18, v15
	v_cmp_eq_u32_e32 vcc, s89, v18
	s_cbranch_vccnz .LBB0_293
	s_and_b32 s12, s18, 0xff
	s_cmp_eq_u32 s12, 0
	s_mov_b64 s[12:13], -1
	s_mov_b64 s[16:17], -1
	s_sleep 4
	s_cbranch_scc0 .LBB0_298
	global_load_dword v18, v17, s[28:29] offset:512 sc1
	s_waitcnt vmcnt(0)
	v_cmp_eq_u32_e32 vcc, 0, v18
	s_cbranch_vccnz .LBB0_300
	s_mov_b64 s[16:17], 0

.LBB0_308:
	s_and_b32 s18, s21, 0xff
	s_mov_b64 s[16:17], -1
	s_cmp_lg_u32 s18, 0
	s_mov_b64 s[22:23], -1
	s_sleep 4
	s_cbranch_scc1 .LBB0_311
	global_load_dword v3, v1, s[28:29] offset:512 sc1
	s_waitcnt vmcnt(0)
	v_cmp_eq_u32_e32 vcc, 0, v3
	s_cbranch_vccnz .LBB0_313
	s_mov_b64 s[22:23], 0
	s_mov_b64 s[18:19], -1

.LBB0_322:
	s_and_b32 s18, s21, 0xff
	s_cmp_lg_u32 s18, 0
	s_mov_b64 s[22:23], -1
	s_sleep 4
	s_cbranch_scc1 .LBB0_325
	global_load_dword v2, v1, s[10:11] sc1
	s_waitcnt vmcnt(0)
	v_cmp_eq_u32_e32 vcc, 0, v2
	s_cbranch_vccnz .LBB0_327
	s_mov_b64 s[22:23], 0
	s_mov_b64 s[18:19], -1

.LBB0_471:
	global_load_dword v16, v17, s[76:77] offset:1024 sc1
	s_waitcnt lgkmcnt(0)
	global_load_dword v1, v17, s[76:77] offset:1280 sc1
	global_load_dword v2, v17, s[76:77] offset:1536 sc1
	global_load_dword v3, v17, s[76:77] offset:1792 sc1
	global_load_dword v4, v17, s[76:77] offset:2048 sc1
	global_load_dword v5, v17, s[76:77] offset:2304 sc1
	global_load_dword v6, v17, s[76:77] offset:2560 sc1
	global_load_dword v7, v17, s[76:77] offset:2816 sc1
	global_load_dword v8, v17, s[76:77] offset:3072 sc1
	global_load_dword v9, v17, s[76:77] offset:3328 sc1
	global_load_dword v10, v17, s[76:77] offset:3584 sc1
	global_load_dword v11, v17, s[76:77] offset:3840 sc1
	global_load_dword v12, v17, s[4:5] sc1
	global_load_dword v13, v17, s[6:7] sc1
	global_load_dword v14, v17, s[8:9] sc1
	global_load_dword v15, v17, s[10:11] sc1
	s_mov_b64 s[12:13], -1
	s_mov_b64 s[14:15], -1
	s_waitcnt vmcnt(14)
	v_add_u32_e32 v18, v1, v16
	s_waitcnt vmcnt(13)
	v_add_u32_e32 v18, v18, v2
	s_waitcnt vmcnt(12)
	v_add_u32_e32 v18, v18, v3
	s_waitcnt vmcnt(11)
	v_add_u32_e32 v18, v18, v4
	s_waitcnt vmcnt(10)
	v_add_u32_e32 v18, v18, v5
	s_waitcnt vmcnt(9)
	v_add_u32_e32 v18, v18, v6
	s_waitcnt vmcnt(8)
	v_add_u32_e32 v18, v18, v7
	s_waitcnt vmcnt(7)
	v_add_u32_e32 v18, v18, v8
	s_waitcnt vmcnt(6)
	v_add_u32_e32 v18, v18, v9
	s_waitcnt vmcnt(5)
	v_add_u32_e32 v18, v18, v10
	s_waitcnt vmcnt(4)
	v_add_u32_e32 v18, v18, v11
	s_waitcnt vmcnt(3)
	v_add_u32_e32 v18, v18, v12
	s_waitcnt vmcnt(2)
	v_add_u32_e32 v18, v18, v13
	s_waitcnt vmcnt(1)
	v_add_u32_e32 v18, v18, v14
	s_waitcnt vmcnt(0)
	v_add_u32_e32 v18, v18, v15
	v_cmp_eq_u32_e32 vcc, s33, v18
	s_cbranch_vccnz .LBB0_470
	s_and_b32 s12, s3, 0xff
	s_cmp_eq_u32 s12, 0
	s_mov_b64 s[12:13], -1
	s_mov_b64 s[16:17], -1
	s_sleep 4
	s_cbranch_scc0 .LBB0_475
	global_load_dword v18, v17, s[76:77] offset:512 sc1
	s_waitcnt vmcnt(0)
	v_cmp_eq_u32_e32 vcc, 0, v18
	s_cbranch_vccnz .LBB0_477
	s_mov_b64 s[16:17], 0

.LBB0_489:
	s_and_b32 s18, s3, 0xff
	s_mov_b64 s[16:17], -1
	s_cmp_lg_u32 s18, 0
	s_mov_b64 s[20:21], -1
	s_sleep 4
	s_cbranch_scc1 .LBB0_492
	global_load_dword v3, v1, s[76:77] offset:512 sc1
	s_waitcnt vmcnt(0)
	v_cmp_eq_u32_e32 vcc, 0, v3
	s_cbranch_vccnz .LBB0_494
	s_mov_b64 s[20:21], 0
	s_mov_b64 s[18:19], -1

.LBB0_506:
	s_and_b32 s18, s3, 0xff
	s_cmp_lg_u32 s18, 0
	s_mov_b64 s[20:21], -1
	s_sleep 4
	s_cbranch_scc1 .LBB0_509
	global_load_dword v2, v1, s[10:11] sc1
	s_waitcnt vmcnt(0)
	v_cmp_eq_u32_e32 vcc, 0, v2
	s_cbranch_vccnz .LBB0_511
	s_mov_b64 s[20:21], 0
	s_mov_b64 s[18:19], -1

.LBB0_1116:
	global_load_dword v15, v16, s[76:77] offset:1024 sc1
	s_waitcnt lgkmcnt(0)
	global_load_dword v0, v16, s[76:77] offset:1280 sc1
	global_load_dword v1, v16, s[76:77] offset:1536 sc1
	global_load_dword v2, v16, s[76:77] offset:1792 sc1
	global_load_dword v3, v16, s[76:77] offset:2048 sc1
	global_load_dword v4, v16, s[76:77] offset:2304 sc1
	global_load_dword v5, v16, s[76:77] offset:2560 sc1
	global_load_dword v6, v16, s[76:77] offset:2816 sc1
	global_load_dword v7, v16, s[76:77] offset:3072 sc1
	global_load_dword v8, v16, s[76:77] offset:3328 sc1
	global_load_dword v9, v16, s[76:77] offset:3584 sc1
	global_load_dword v10, v16, s[76:77] offset:3840 sc1
	global_load_dword v11, v16, s[4:5] sc1
	global_load_dword v12, v16, s[6:7] sc1
	global_load_dword v13, v16, s[8:9] sc1
	global_load_dword v14, v16, s[10:11] sc1
	s_mov_b64 s[12:13], -1
	s_mov_b64 s[14:15], -1
	s_waitcnt vmcnt(14)
	v_add_u32_e32 v17, v0, v15
	s_waitcnt vmcnt(13)
	v_add_u32_e32 v17, v17, v1
	s_waitcnt vmcnt(12)
	v_add_u32_e32 v17, v17, v2
	s_waitcnt vmcnt(11)
	v_add_u32_e32 v17, v17, v3
	s_waitcnt vmcnt(10)
	v_add_u32_e32 v17, v17, v4
	s_waitcnt vmcnt(9)
	v_add_u32_e32 v17, v17, v5
	s_waitcnt vmcnt(8)
	v_add_u32_e32 v17, v17, v6
	s_waitcnt vmcnt(7)
	v_add_u32_e32 v17, v17, v7
	s_waitcnt vmcnt(6)
	v_add_u32_e32 v17, v17, v8
	s_waitcnt vmcnt(5)
	v_add_u32_e32 v17, v17, v9
	s_waitcnt vmcnt(4)
	v_add_u32_e32 v17, v17, v10
	s_waitcnt vmcnt(3)
	v_add_u32_e32 v17, v17, v11
	s_waitcnt vmcnt(2)
	v_add_u32_e32 v17, v17, v12
	s_waitcnt vmcnt(1)
	v_add_u32_e32 v17, v17, v13
	s_waitcnt vmcnt(0)
	v_add_u32_e32 v17, v17, v14
	v_cmp_eq_u32_e32 vcc, s33, v17
	s_cbranch_vccnz .LBB0_1115
	s_and_b32 s12, s3, 0xff
	s_cmp_eq_u32 s12, 0
	s_mov_b64 s[12:13], -1
	s_mov_b64 s[16:17], -1
	s_sleep 4
	s_cbranch_scc0 .LBB0_1120
	global_load_dword v17, v16, s[76:77] offset:512 sc1
	s_waitcnt vmcnt(0)
	v_cmp_eq_u32_e32 vcc, 0, v17
	s_cbranch_vccnz .LBB0_1122
	s_mov_b64 s[16:17], 0

.LBB0_1134:
	s_and_b32 s18, s3, 0xff
	s_mov_b64 s[16:17], -1
	s_cmp_lg_u32 s18, 0
	s_mov_b64 s[20:21], -1
	s_sleep 4
	s_cbranch_scc1 .LBB0_1137
	global_load_dword v2, v0, s[76:77] offset:512 sc1
	s_waitcnt vmcnt(0)
	v_cmp_eq_u32_e32 vcc, 0, v2
	s_cbranch_vccnz .LBB0_1139
	s_mov_b64 s[20:21], 0
	s_mov_b64 s[18:19], -1

.LBB0_1151:
	s_and_b32 s18, s3, 0xff
	s_cmp_lg_u32 s18, 0
	s_mov_b64 s[20:21], -1
	s_sleep 4
	s_cbranch_scc1 .LBB0_1154
	global_load_dword v1, v0, s[10:11] sc1
	s_waitcnt vmcnt(0)
	v_cmp_eq_u32_e32 vcc, 0, v1
	s_cbranch_vccnz .LBB0_1156
	s_mov_b64 s[20:21], 0
	s_mov_b64 s[18:19], -1
